# refine unit: W1 rows staged through wave-private LDS by LDS-DMA (12 loads per 32 k instead of 24), K/V three groups ahead
# baseline (speedup 1.0000x reference)
.Lrg_slow:
	s_getpc_b64 s[4:5]
	s_and_b32 s4, s4, -16
	v_lshlrev_b32_e32 v2, 4, v1
	global_load_dwordx4 v[100:103], v2, s[4:5] offset:0
	global_load_dwordx4 v[104:107], v2, s[4:5] offset:1024
	global_load_dwordx4 v[108:111], v2, s[4:5] offset:2048
	global_load_dwordx4 v[112:115], v2, s[4:5] offset:3072
	s_add_u32 s4, s4, 0x1000
	s_addc_u32 s5, s5, 0
	global_load_dwordx4 v[116:119], v2, s[4:5] offset:0
	global_load_dwordx4 v[120:123], v2, s[4:5] offset:1024
	global_load_dwordx4 v[124:127], v2, s[4:5] offset:2048
	global_load_dwordx4 v[128:131], v2, s[4:5] offset:3072
	s_add_u32 s4, s4, 0x1000
	s_addc_u32 s5, s5, 0
	global_load_dwordx4 v[100:103], v2, s[4:5] offset:0
	global_load_dwordx4 v[104:107], v2, s[4:5] offset:1024
	global_load_dwordx4 v[108:111], v2, s[4:5] offset:2048
	global_load_dwordx4 v[112:115], v2, s[4:5] offset:3072
	s_add_u32 s4, s4, 0x1000
	s_addc_u32 s5, s5, 0
	global_load_dwordx4 v[116:119], v2, s[4:5] offset:0
	global_load_dwordx4 v[120:123], v2, s[4:5] offset:1024
	s_mov_b32 s3, s24
	s_mov_b32 s33, s27
	v_mov_b32_e32 v26, v1
	v_cmp_gt_u32_e64 s[10:11], 64, v0
	v_mov_b32_e32 v2, s50
	v_mov_b32_e32 v3, s51
	v_mov_b32_e32 v4, s54
	v_mov_b32_e32 v5, s55
	v_mov_b32_e32 v1, 0
	v_cmp_eq_u32_e32 vcc, 0, v0
	s_and_saveexec_b64 s[6:7], vcc
	ds_write_b128 v1, v[2:5] offset:16400

.LBB2_14:
	s_and_b32 s28, s34, 15
	s_ff1_i32_b64 s37, s[30:31]
	s_lshl_b32 s28, s28, 7
	v_lshl_add_u64 v[14:15], v[4:5], 0, s[28:29]
	v_lshl_add_u64 v[16:17], v[6:7], 0, s[28:29]
	v_lshl_add_u64 v[18:19], v[8:9], 0, s[28:29]
	v_lshl_add_u64 v[20:21], v[10:11], 0, s[28:29]
	s_add_i32 s28, s39, s37
	s_lshl_b32 s30, s34, 1
	v_lshl_or_b32 v22, s28, 6, v2
	v_and_or_b32 v22, s30, 32, v22
	v_mov_b32_e32 v23, v1
	v_lshlrev_b64 v[24:25], 12, v[22:23]
	s_and_b32 s36, s34, 31
	v_lshl_add_u64 v[22:23], s[12:13], 0, v[24:25]
	v_lshl_add_u64 v[24:25], s[14:15], 0, v[24:25]
	v_accvgpr_write_b32 a15, 0
	v_accvgpr_write_b32 a14, 0
	v_accvgpr_write_b32 a13, 0
	v_accvgpr_write_b32 a12, 0
	v_accvgpr_write_b32 a11, 0
	v_accvgpr_write_b32 a10, 0
	v_accvgpr_write_b32 a9, 0
	v_accvgpr_write_b32 a8, 0
	v_accvgpr_write_b32 a7, 0
	v_accvgpr_write_b32 a6, 0
	v_accvgpr_write_b32 a5, 0
	v_accvgpr_write_b32 a4, 0
	v_accvgpr_write_b32 a3, 0
	v_accvgpr_write_b32 a2, 0
	v_accvgpr_write_b32 a1, 0
	v_accvgpr_write_b32 a0, 0
	s_mov_b64 s[30:31], 0
	v_lshl_add_u64 v[182:183], v[22:23], 0, v[12:13]
	v_lshl_add_u64 v[184:185], v[24:25], 0, v[12:13]
	v_readfirstlane_b32 s30, v16
	v_readfirstlane_b32 s31, v17
	v_readfirstlane_b32 s41, v0
	v_lshrrev_b32_e32 v191, 3, v26
	v_and_b32_e32 v186, 7, v26
	v_lshlrev_b32_e32 v191, 11, v191
	v_lshl_or_b32 v186, v186, 4, v191
	v_mov_b32_e32 v187, 0
	v_lshl_add_u64 v[188:189], v[186:187], 0, s[30:31]
	s_lshr_b32 s41, s41, 6
	s_mul_i32 s40, s41, 12288
	s_add_i32 s40, s40, 16448
	s_mov_b32 s43, 0
	v_lshrrev_b32_e32 v191, 5, v26
	v_and_b32_e32 v190, 31, v26
	v_lshlrev_b32_e32 v191, 9, v191
	v_lshl_or_b32 v190, v190, 2, v191
	v_add_u32_e32 v190, s40, v190
	s_add_i32 s28, s40, 0
	s_mov_b32 s42, 0x0
	s_mov_b32 m0, s28
	v_lshl_add_u64 v[186:187], v[188:189], 0, s[42:43]
	global_load_lds_dwordx4 v[186:187], off
	s_add_i32 s28, s40, 1024
	s_mov_b32 s42, 0x4000
	s_mov_b32 m0, s28
	v_lshl_add_u64 v[186:187], v[188:189], 0, s[42:43]
	global_load_lds_dwordx4 v[186:187], off
	s_add_i32 s28, s40, 2048
	s_mov_b32 s42, 0x8000
	s_mov_b32 m0, s28
	v_lshl_add_u64 v[186:187], v[188:189], 0, s[42:43]
	global_load_lds_dwordx4 v[186:187], off
	s_add_i32 s28, s40, 3072
	s_mov_b32 s42, 0xc000
	s_mov_b32 m0, s28
	v_lshl_add_u64 v[186:187], v[188:189], 0, s[42:43]
	global_load_lds_dwordx4 v[186:187], off
	global_load_dwordx4 v[38:41], v[182:183], off offset:0
	global_load_dwordx4 v[54:57], v[184:185], off offset:0
	global_load_dwordx4 v[42:45], v[182:183], off offset:32
	global_load_dwordx4 v[58:61], v[184:185], off offset:32
	global_load_dwordx4 v[46:49], v[182:183], off offset:64
	global_load_dwordx4 v[62:65], v[184:185], off offset:64
	global_load_dwordx4 v[50:53], v[182:183], off offset:96
	global_load_dwordx4 v[66:69], v[184:185], off offset:96
	s_add_i32 s28, s40, 4096
	s_mov_b32 s42, 0x10000
	s_mov_b32 m0, s28
	v_lshl_add_u64 v[186:187], v[188:189], 0, s[42:43]
	global_load_lds_dwordx4 v[186:187], off
	s_add_i32 s28, s40, 5120
	s_mov_b32 s42, 0x14000
	s_mov_b32 m0, s28
	v_lshl_add_u64 v[186:187], v[188:189], 0, s[42:43]
	global_load_lds_dwordx4 v[186:187], off
	s_add_i32 s28, s40, 6144
	s_mov_b32 s42, 0x18000
	s_mov_b32 m0, s28
	v_lshl_add_u64 v[186:187], v[188:189], 0, s[42:43]
	global_load_lds_dwordx4 v[186:187], off
	s_add_i32 s28, s40, 7168
	s_mov_b32 s42, 0x1c000
	s_mov_b32 m0, s28
	v_lshl_add_u64 v[186:187], v[188:189], 0, s[42:43]
	global_load_lds_dwordx4 v[186:187], off
	global_load_dwordx4 v[70:73], v[182:183], off offset:128
	global_load_dwordx4 v[86:89], v[184:185], off offset:128
	global_load_dwordx4 v[74:77], v[182:183], off offset:160
	global_load_dwordx4 v[90:93], v[184:185], off offset:160
	global_load_dwordx4 v[78:81], v[182:183], off offset:192
	global_load_dwordx4 v[94:97], v[184:185], off offset:192
	global_load_dwordx4 v[82:85], v[182:183], off offset:224
	global_load_dwordx4 v[98:101], v[184:185], off offset:224
	global_load_dwordx4 v[102:105], v[182:183], off offset:256
	global_load_dwordx4 v[118:121], v[184:185], off offset:256
	global_load_dwordx4 v[106:109], v[182:183], off offset:288
	global_load_dwordx4 v[122:125], v[184:185], off offset:288
	global_load_dwordx4 v[110:113], v[182:183], off offset:320
	global_load_dwordx4 v[126:129], v[184:185], off offset:320
	global_load_dwordx4 v[114:117], v[182:183], off offset:352
	global_load_dwordx4 v[130:133], v[184:185], off offset:352
	s_waitcnt vmcnt(28)
	s_waitcnt vmcnt(20)
	ds_read_b32 v166, v190 offset:0
	ds_read_b32 v167, v190 offset:128
	ds_read_b32 v168, v190 offset:256
	ds_read_b32 v169, v190 offset:384
	ds_read_b32 v170, v190 offset:1024
	ds_read_b32 v171, v190 offset:1152
	ds_read_b32 v172, v190 offset:1280
	ds_read_b32 v173, v190 offset:1408
	ds_read_b32 v174, v190 offset:2048
	ds_read_b32 v175, v190 offset:2176
	ds_read_b32 v176, v190 offset:2304
	ds_read_b32 v177, v190 offset:2432
	ds_read_b32 v178, v190 offset:3072
	ds_read_b32 v179, v190 offset:3200
	ds_read_b32 v180, v190 offset:3328
	ds_read_b32 v181, v190 offset:3456
	s_add_i32 s28, s40, 8192
	s_mov_b32 s42, 0x20000
	s_mov_b32 m0, s28
	v_lshl_add_u64 v[186:187], v[188:189], 0, s[42:43]
	global_load_lds_dwordx4 v[186:187], off
	s_add_i32 s28, s40, 9216
	s_mov_b32 s42, 0x24000
	s_mov_b32 m0, s28
	v_lshl_add_u64 v[186:187], v[188:189], 0, s[42:43]
	global_load_lds_dwordx4 v[186:187], off
	s_add_i32 s28, s40, 10240
	s_mov_b32 s42, 0x28000
	s_mov_b32 m0, s28
	v_lshl_add_u64 v[186:187], v[188:189], 0, s[42:43]
	global_load_lds_dwordx4 v[186:187], off
	s_add_i32 s28, s40, 11264
	s_mov_b32 s42, 0x2c000
	s_mov_b32 m0, s28
	v_lshl_add_u64 v[186:187], v[188:189], 0, s[42:43]
	global_load_lds_dwordx4 v[186:187], off
	global_load_dwordx4 v[134:137], v[182:183], off offset:384
	global_load_dwordx4 v[150:153], v[184:185], off offset:384
	global_load_dwordx4 v[138:141], v[182:183], off offset:416
	global_load_dwordx4 v[154:157], v[184:185], off offset:416
	global_load_dwordx4 v[142:145], v[182:183], off offset:448
	global_load_dwordx4 v[158:161], v[184:185], off offset:448
	global_load_dwordx4 v[146:149], v[182:183], off offset:480
	global_load_dwordx4 v[162:165], v[184:185], off offset:480
	v_add_f32_e32 v38, v38, v54
	v_mul_f32_e32 v38, 0.5, v38
	v_add_f32_e32 v39, v39, v55
	v_mul_f32_e32 v39, 0.5, v39
	v_add_f32_e32 v40, v40, v56
	v_mul_f32_e32 v40, 0.5, v40
	s_waitcnt lgkmcnt(15)
	v_mfma_f32_32x32x2_f32 a[0:15], v38, v166, a[0:15]
	v_add_f32_e32 v41, v41, v57
	v_mul_f32_e32 v41, 0.5, v41
	s_waitcnt lgkmcnt(14)
	v_mfma_f32_32x32x2_f32 a[0:15], v39, v167, a[0:15]
	v_add_f32_e32 v42, v42, v58
	v_mul_f32_e32 v42, 0.5, v42
	s_waitcnt lgkmcnt(13)
	v_mfma_f32_32x32x2_f32 a[0:15], v40, v168, a[0:15]
	v_add_f32_e32 v43, v43, v59
	v_mul_f32_e32 v43, 0.5, v43
	s_waitcnt lgkmcnt(12)
	v_mfma_f32_32x32x2_f32 a[0:15], v41, v169, a[0:15]
	v_add_f32_e32 v44, v44, v60
	v_mul_f32_e32 v44, 0.5, v44
	s_waitcnt lgkmcnt(11)
	v_mfma_f32_32x32x2_f32 a[0:15], v42, v170, a[0:15]
	v_add_f32_e32 v45, v45, v61
	v_mul_f32_e32 v45, 0.5, v45
	s_waitcnt lgkmcnt(10)
	v_mfma_f32_32x32x2_f32 a[0:15], v43, v171, a[0:15]
	v_add_f32_e32 v46, v46, v62
	v_mul_f32_e32 v46, 0.5, v46
	s_waitcnt lgkmcnt(9)
	v_mfma_f32_32x32x2_f32 a[0:15], v44, v172, a[0:15]
	v_add_f32_e32 v47, v47, v63
	v_mul_f32_e32 v47, 0.5, v47
	s_waitcnt lgkmcnt(8)
	v_mfma_f32_32x32x2_f32 a[0:15], v45, v173, a[0:15]
	v_add_f32_e32 v48, v48, v64
	v_mul_f32_e32 v48, 0.5, v48
	s_waitcnt lgkmcnt(7)
	v_mfma_f32_32x32x2_f32 a[0:15], v46, v174, a[0:15]
	v_add_f32_e32 v49, v49, v65
	v_mul_f32_e32 v49, 0.5, v49
	s_waitcnt lgkmcnt(6)
	v_mfma_f32_32x32x2_f32 a[0:15], v47, v175, a[0:15]
	v_add_f32_e32 v50, v50, v66
	v_mul_f32_e32 v50, 0.5, v50
	s_waitcnt lgkmcnt(5)
	v_mfma_f32_32x32x2_f32 a[0:15], v48, v176, a[0:15]
	v_add_f32_e32 v51, v51, v67
	v_mul_f32_e32 v51, 0.5, v51
	s_waitcnt lgkmcnt(4)
	v_mfma_f32_32x32x2_f32 a[0:15], v49, v177, a[0:15]
	v_add_f32_e32 v52, v52, v68
	v_mul_f32_e32 v52, 0.5, v52
	s_waitcnt lgkmcnt(3)
	v_mfma_f32_32x32x2_f32 a[0:15], v50, v178, a[0:15]
	v_add_f32_e32 v53, v53, v69
	v_mul_f32_e32 v53, 0.5, v53
	s_waitcnt lgkmcnt(2)
	v_mfma_f32_32x32x2_f32 a[0:15], v51, v179, a[0:15]
	s_waitcnt lgkmcnt(1)
	v_mfma_f32_32x32x2_f32 a[0:15], v52, v180, a[0:15]
	s_waitcnt lgkmcnt(0)
	v_mfma_f32_32x32x2_f32 a[0:15], v53, v181, a[0:15]
	s_waitcnt vmcnt(28)
	s_waitcnt vmcnt(20)
	ds_read_b32 v166, v190 offset:4096
	ds_read_b32 v167, v190 offset:4224
	ds_read_b32 v168, v190 offset:4352
	ds_read_b32 v169, v190 offset:4480
	ds_read_b32 v170, v190 offset:5120
	ds_read_b32 v171, v190 offset:5248
	ds_read_b32 v172, v190 offset:5376
	ds_read_b32 v173, v190 offset:5504
	ds_read_b32 v174, v190 offset:6144
	ds_read_b32 v175, v190 offset:6272
	ds_read_b32 v176, v190 offset:6400
	ds_read_b32 v177, v190 offset:6528
	ds_read_b32 v178, v190 offset:7168
	ds_read_b32 v179, v190 offset:7296
	ds_read_b32 v180, v190 offset:7424
	ds_read_b32 v181, v190 offset:7552
	s_add_i32 s28, s40, 0
	s_mov_b32 s42, 0x30000
	s_mov_b32 m0, s28
	v_lshl_add_u64 v[186:187], v[188:189], 0, s[42:43]
	global_load_lds_dwordx4 v[186:187], off
	s_add_i32 s28, s40, 1024
	s_mov_b32 s42, 0x34000
	s_mov_b32 m0, s28
	v_lshl_add_u64 v[186:187], v[188:189], 0, s[42:43]
	global_load_lds_dwordx4 v[186:187], off
	s_add_i32 s28, s40, 2048
	s_mov_b32 s42, 0x38000
	s_mov_b32 m0, s28
	v_lshl_add_u64 v[186:187], v[188:189], 0, s[42:43]
	global_load_lds_dwordx4 v[186:187], off
	s_add_i32 s28, s40, 3072
	s_mov_b32 s42, 0x3c000
	s_mov_b32 m0, s28
	v_lshl_add_u64 v[186:187], v[188:189], 0, s[42:43]
	global_load_lds_dwordx4 v[186:187], off
	global_load_dwordx4 v[38:41], v[182:183], off offset:512
	global_load_dwordx4 v[54:57], v[184:185], off offset:512
	global_load_dwordx4 v[42:45], v[182:183], off offset:544
	global_load_dwordx4 v[58:61], v[184:185], off offset:544
	global_load_dwordx4 v[46:49], v[182:183], off offset:576
	global_load_dwordx4 v[62:65], v[184:185], off offset:576
	global_load_dwordx4 v[50:53], v[182:183], off offset:608
	global_load_dwordx4 v[66:69], v[184:185], off offset:608
	v_add_f32_e32 v70, v70, v86
	v_mul_f32_e32 v70, 0.5, v70
	v_add_f32_e32 v71, v71, v87
	v_mul_f32_e32 v71, 0.5, v71
	v_add_f32_e32 v72, v72, v88
	v_mul_f32_e32 v72, 0.5, v72
	s_waitcnt lgkmcnt(15)
	v_mfma_f32_32x32x2_f32 a[0:15], v70, v166, a[0:15]
	v_add_f32_e32 v73, v73, v89
	v_mul_f32_e32 v73, 0.5, v73
	s_waitcnt lgkmcnt(14)
	v_mfma_f32_32x32x2_f32 a[0:15], v71, v167, a[0:15]
	v_add_f32_e32 v74, v74, v90
	v_mul_f32_e32 v74, 0.5, v74
	s_waitcnt lgkmcnt(13)
	v_mfma_f32_32x32x2_f32 a[0:15], v72, v168, a[0:15]
	v_add_f32_e32 v75, v75, v91
	v_mul_f32_e32 v75, 0.5, v75
	s_waitcnt lgkmcnt(12)
	v_mfma_f32_32x32x2_f32 a[0:15], v73, v169, a[0:15]
	v_add_f32_e32 v76, v76, v92
	v_mul_f32_e32 v76, 0.5, v76
	s_waitcnt lgkmcnt(11)
	v_mfma_f32_32x32x2_f32 a[0:15], v74, v170, a[0:15]
	v_add_f32_e32 v77, v77, v93
	v_mul_f32_e32 v77, 0.5, v77
	s_waitcnt lgkmcnt(10)
	v_mfma_f32_32x32x2_f32 a[0:15], v75, v171, a[0:15]
	v_add_f32_e32 v78, v78, v94
	v_mul_f32_e32 v78, 0.5, v78
	s_waitcnt lgkmcnt(9)
	v_mfma_f32_32x32x2_f32 a[0:15], v76, v172, a[0:15]
	v_add_f32_e32 v79, v79, v95
	v_mul_f32_e32 v79, 0.5, v79
	s_waitcnt lgkmcnt(8)
	v_mfma_f32_32x32x2_f32 a[0:15], v77, v173, a[0:15]
	v_add_f32_e32 v80, v80, v96
	v_mul_f32_e32 v80, 0.5, v80
	s_waitcnt lgkmcnt(7)
	v_mfma_f32_32x32x2_f32 a[0:15], v78, v174, a[0:15]
	v_add_f32_e32 v81, v81, v97
	v_mul_f32_e32 v81, 0.5, v81
	s_waitcnt lgkmcnt(6)
	v_mfma_f32_32x32x2_f32 a[0:15], v79, v175, a[0:15]
	v_add_f32_e32 v82, v82, v98
	v_mul_f32_e32 v82, 0.5, v82
	s_waitcnt lgkmcnt(5)
	v_mfma_f32_32x32x2_f32 a[0:15], v80, v176, a[0:15]
	v_add_f32_e32 v83, v83, v99
	v_mul_f32_e32 v83, 0.5, v83
	s_waitcnt lgkmcnt(4)
	v_mfma_f32_32x32x2_f32 a[0:15], v81, v177, a[0:15]
	v_add_f32_e32 v84, v84, v100
	v_mul_f32_e32 v84, 0.5, v84
	s_waitcnt lgkmcnt(3)
	v_mfma_f32_32x32x2_f32 a[0:15], v82, v178, a[0:15]
	v_add_f32_e32 v85, v85, v101
	v_mul_f32_e32 v85, 0.5, v85
	s_waitcnt lgkmcnt(2)
	v_mfma_f32_32x32x2_f32 a[0:15], v83, v179, a[0:15]
	s_waitcnt lgkmcnt(1)
	v_mfma_f32_32x32x2_f32 a[0:15], v84, v180, a[0:15]
	s_waitcnt lgkmcnt(0)
	v_mfma_f32_32x32x2_f32 a[0:15], v85, v181, a[0:15]
	s_waitcnt vmcnt(20)
	ds_read_b32 v166, v190 offset:8192
	ds_read_b32 v167, v190 offset:8320
	ds_read_b32 v168, v190 offset:8448
	ds_read_b32 v169, v190 offset:8576
	ds_read_b32 v170, v190 offset:9216
	ds_read_b32 v171, v190 offset:9344
	ds_read_b32 v172, v190 offset:9472
	ds_read_b32 v173, v190 offset:9600
	ds_read_b32 v174, v190 offset:10240
	ds_read_b32 v175, v190 offset:10368
	ds_read_b32 v176, v190 offset:10496
	ds_read_b32 v177, v190 offset:10624
	ds_read_b32 v178, v190 offset:11264
	ds_read_b32 v179, v190 offset:11392
	ds_read_b32 v180, v190 offset:11520
	ds_read_b32 v181, v190 offset:11648
	s_add_i32 s28, s40, 4096
	s_mov_b32 s42, 0x40000
	s_mov_b32 m0, s28
	v_lshl_add_u64 v[186:187], v[188:189], 0, s[42:43]
	global_load_lds_dwordx4 v[186:187], off
	s_add_i32 s28, s40, 5120
	s_mov_b32 s42, 0x44000
	s_mov_b32 m0, s28
	v_lshl_add_u64 v[186:187], v[188:189], 0, s[42:43]
	global_load_lds_dwordx4 v[186:187], off
	s_add_i32 s28, s40, 6144
	s_mov_b32 s42, 0x48000
	s_mov_b32 m0, s28
	v_lshl_add_u64 v[186:187], v[188:189], 0, s[42:43]
	global_load_lds_dwordx4 v[186:187], off
	s_add_i32 s28, s40, 7168
	s_mov_b32 s42, 0x4c000
	s_mov_b32 m0, s28
	v_lshl_add_u64 v[186:187], v[188:189], 0, s[42:43]
	global_load_lds_dwordx4 v[186:187], off
	global_load_dwordx4 v[70:73], v[182:183], off offset:640
	global_load_dwordx4 v[86:89], v[184:185], off offset:640
	global_load_dwordx4 v[74:77], v[182:183], off offset:672
	global_load_dwordx4 v[90:93], v[184:185], off offset:672
	global_load_dwordx4 v[78:81], v[182:183], off offset:704
	global_load_dwordx4 v[94:97], v[184:185], off offset:704
	global_load_dwordx4 v[82:85], v[182:183], off offset:736
	global_load_dwordx4 v[98:101], v[184:185], off offset:736
	v_add_f32_e32 v102, v102, v118
	v_mul_f32_e32 v102, 0.5, v102
	v_add_f32_e32 v103, v103, v119
	v_mul_f32_e32 v103, 0.5, v103
	v_add_f32_e32 v104, v104, v120
	v_mul_f32_e32 v104, 0.5, v104
	s_waitcnt lgkmcnt(15)
	v_mfma_f32_32x32x2_f32 a[0:15], v102, v166, a[0:15]
	v_add_f32_e32 v105, v105, v121
	v_mul_f32_e32 v105, 0.5, v105
	s_waitcnt lgkmcnt(14)
	v_mfma_f32_32x32x2_f32 a[0:15], v103, v167, a[0:15]
	v_add_f32_e32 v106, v106, v122
	v_mul_f32_e32 v106, 0.5, v106
	s_waitcnt lgkmcnt(13)
	v_mfma_f32_32x32x2_f32 a[0:15], v104, v168, a[0:15]
	v_add_f32_e32 v107, v107, v123
	v_mul_f32_e32 v107, 0.5, v107
	s_waitcnt lgkmcnt(12)
	v_mfma_f32_32x32x2_f32 a[0:15], v105, v169, a[0:15]
	v_add_f32_e32 v108, v108, v124
	v_mul_f32_e32 v108, 0.5, v108
	s_waitcnt lgkmcnt(11)
	v_mfma_f32_32x32x2_f32 a[0:15], v106, v170, a[0:15]
	v_add_f32_e32 v109, v109, v125
	v_mul_f32_e32 v109, 0.5, v109
	s_waitcnt lgkmcnt(10)
	v_mfma_f32_32x32x2_f32 a[0:15], v107, v171, a[0:15]
	v_add_f32_e32 v110, v110, v126
	v_mul_f32_e32 v110, 0.5, v110
	s_waitcnt lgkmcnt(9)
	v_mfma_f32_32x32x2_f32 a[0:15], v108, v172, a[0:15]
	v_add_f32_e32 v111, v111, v127
	v_mul_f32_e32 v111, 0.5, v111
	s_waitcnt lgkmcnt(8)
	v_mfma_f32_32x32x2_f32 a[0:15], v109, v173, a[0:15]
	v_add_f32_e32 v112, v112, v128
	v_mul_f32_e32 v112, 0.5, v112
	s_waitcnt lgkmcnt(7)
	v_mfma_f32_32x32x2_f32 a[0:15], v110, v174, a[0:15]
	v_add_f32_e32 v113, v113, v129
	v_mul_f32_e32 v113, 0.5, v113
	s_waitcnt lgkmcnt(6)
	v_mfma_f32_32x32x2_f32 a[0:15], v111, v175, a[0:15]
	v_add_f32_e32 v114, v114, v130
	v_mul_f32_e32 v114, 0.5, v114
	s_waitcnt lgkmcnt(5)
	v_mfma_f32_32x32x2_f32 a[0:15], v112, v176, a[0:15]
	v_add_f32_e32 v115, v115, v131
	v_mul_f32_e32 v115, 0.5, v115
	s_waitcnt lgkmcnt(4)
	v_mfma_f32_32x32x2_f32 a[0:15], v113, v177, a[0:15]
	v_add_f32_e32 v116, v116, v132
	v_mul_f32_e32 v116, 0.5, v116
	s_waitcnt lgkmcnt(3)
	v_mfma_f32_32x32x2_f32 a[0:15], v114, v178, a[0:15]
	v_add_f32_e32 v117, v117, v133
	v_mul_f32_e32 v117, 0.5, v117
	s_waitcnt lgkmcnt(2)
	v_mfma_f32_32x32x2_f32 a[0:15], v115, v179, a[0:15]
	s_waitcnt lgkmcnt(1)
	v_mfma_f32_32x32x2_f32 a[0:15], v116, v180, a[0:15]
	s_waitcnt lgkmcnt(0)
	v_mfma_f32_32x32x2_f32 a[0:15], v117, v181, a[0:15]
	s_waitcnt vmcnt(20)
	ds_read_b32 v166, v190 offset:0
	ds_read_b32 v167, v190 offset:128
	ds_read_b32 v168, v190 offset:256
	ds_read_b32 v169, v190 offset:384
	ds_read_b32 v170, v190 offset:1024
	ds_read_b32 v171, v190 offset:1152
	ds_read_b32 v172, v190 offset:1280
	ds_read_b32 v173, v190 offset:1408
	ds_read_b32 v174, v190 offset:2048
	ds_read_b32 v175, v190 offset:2176
	ds_read_b32 v176, v190 offset:2304
	ds_read_b32 v177, v190 offset:2432
	ds_read_b32 v178, v190 offset:3072
	ds_read_b32 v179, v190 offset:3200
	ds_read_b32 v180, v190 offset:3328
	ds_read_b32 v181, v190 offset:3456
	s_add_i32 s28, s40, 8192
	s_mov_b32 s42, 0x50000
	s_mov_b32 m0, s28
	v_lshl_add_u64 v[186:187], v[188:189], 0, s[42:43]
	global_load_lds_dwordx4 v[186:187], off
	s_add_i32 s28, s40, 9216
	s_mov_b32 s42, 0x54000
	s_mov_b32 m0, s28
	v_lshl_add_u64 v[186:187], v[188:189], 0, s[42:43]
	global_load_lds_dwordx4 v[186:187], off
	s_add_i32 s28, s40, 10240
	s_mov_b32 s42, 0x58000
	s_mov_b32 m0, s28
	v_lshl_add_u64 v[186:187], v[188:189], 0, s[42:43]
	global_load_lds_dwordx4 v[186:187], off
	s_add_i32 s28, s40, 11264
	s_mov_b32 s42, 0x5c000
	s_mov_b32 m0, s28
	v_lshl_add_u64 v[186:187], v[188:189], 0, s[42:43]
	global_load_lds_dwordx4 v[186:187], off
	global_load_dwordx4 v[102:105], v[182:183], off offset:768
	global_load_dwordx4 v[118:121], v[184:185], off offset:768
	global_load_dwordx4 v[106:109], v[182:183], off offset:800
	global_load_dwordx4 v[122:125], v[184:185], off offset:800
	global_load_dwordx4 v[110:113], v[182:183], off offset:832
	global_load_dwordx4 v[126:129], v[184:185], off offset:832
	global_load_dwordx4 v[114:117], v[182:183], off offset:864
	global_load_dwordx4 v[130:133], v[184:185], off offset:864
	v_add_f32_e32 v134, v134, v150
	v_mul_f32_e32 v134, 0.5, v134
	v_add_f32_e32 v135, v135, v151
	v_mul_f32_e32 v135, 0.5, v135
	v_add_f32_e32 v136, v136, v152
	v_mul_f32_e32 v136, 0.5, v136
	s_waitcnt lgkmcnt(15)
	v_mfma_f32_32x32x2_f32 a[0:15], v134, v166, a[0:15]
	v_add_f32_e32 v137, v137, v153
	v_mul_f32_e32 v137, 0.5, v137
	s_waitcnt lgkmcnt(14)
	v_mfma_f32_32x32x2_f32 a[0:15], v135, v167, a[0:15]
	v_add_f32_e32 v138, v138, v154
	v_mul_f32_e32 v138, 0.5, v138
	s_waitcnt lgkmcnt(13)
	v_mfma_f32_32x32x2_f32 a[0:15], v136, v168, a[0:15]
	v_add_f32_e32 v139, v139, v155
	v_mul_f32_e32 v139, 0.5, v139
	s_waitcnt lgkmcnt(12)
	v_mfma_f32_32x32x2_f32 a[0:15], v137, v169, a[0:15]
	v_add_f32_e32 v140, v140, v156
	v_mul_f32_e32 v140, 0.5, v140
	s_waitcnt lgkmcnt(11)
	v_mfma_f32_32x32x2_f32 a[0:15], v138, v170, a[0:15]
	v_add_f32_e32 v141, v141, v157
	v_mul_f32_e32 v141, 0.5, v141
	s_waitcnt lgkmcnt(10)
	v_mfma_f32_32x32x2_f32 a[0:15], v139, v171, a[0:15]
	v_add_f32_e32 v142, v142, v158
	v_mul_f32_e32 v142, 0.5, v142
	s_waitcnt lgkmcnt(9)
	v_mfma_f32_32x32x2_f32 a[0:15], v140, v172, a[0:15]
	v_add_f32_e32 v143, v143, v159
	v_mul_f32_e32 v143, 0.5, v143
	s_waitcnt lgkmcnt(8)
	v_mfma_f32_32x32x2_f32 a[0:15], v141, v173, a[0:15]
	v_add_f32_e32 v144, v144, v160
	v_mul_f32_e32 v144, 0.5, v144
	s_waitcnt lgkmcnt(7)
	v_mfma_f32_32x32x2_f32 a[0:15], v142, v174, a[0:15]
	v_add_f32_e32 v145, v145, v161
	v_mul_f32_e32 v145, 0.5, v145
	s_waitcnt lgkmcnt(6)
	v_mfma_f32_32x32x2_f32 a[0:15], v143, v175, a[0:15]
	v_add_f32_e32 v146, v146, v162
	v_mul_f32_e32 v146, 0.5, v146
	s_waitcnt lgkmcnt(5)
	v_mfma_f32_32x32x2_f32 a[0:15], v144, v176, a[0:15]
	v_add_f32_e32 v147, v147, v163
	v_mul_f32_e32 v147, 0.5, v147
	s_waitcnt lgkmcnt(4)
	v_mfma_f32_32x32x2_f32 a[0:15], v145, v177, a[0:15]
	v_add_f32_e32 v148, v148, v164
	v_mul_f32_e32 v148, 0.5, v148
	s_waitcnt lgkmcnt(3)
	v_mfma_f32_32x32x2_f32 a[0:15], v146, v178, a[0:15]
	v_add_f32_e32 v149, v149, v165
	v_mul_f32_e32 v149, 0.5, v149
	s_waitcnt lgkmcnt(2)
	v_mfma_f32_32x32x2_f32 a[0:15], v147, v179, a[0:15]
	s_waitcnt lgkmcnt(1)
	v_mfma_f32_32x32x2_f32 a[0:15], v148, v180, a[0:15]
	s_waitcnt lgkmcnt(0)
	v_mfma_f32_32x32x2_f32 a[0:15], v149, v181, a[0:15]
	s_waitcnt vmcnt(20)
	ds_read_b32 v166, v190 offset:4096
	ds_read_b32 v167, v190 offset:4224
	ds_read_b32 v168, v190 offset:4352
	ds_read_b32 v169, v190 offset:4480
	ds_read_b32 v170, v190 offset:5120
	ds_read_b32 v171, v190 offset:5248
	ds_read_b32 v172, v190 offset:5376
	ds_read_b32 v173, v190 offset:5504
	ds_read_b32 v174, v190 offset:6144
	ds_read_b32 v175, v190 offset:6272
	ds_read_b32 v176, v190 offset:6400
	ds_read_b32 v177, v190 offset:6528
	ds_read_b32 v178, v190 offset:7168
	ds_read_b32 v179, v190 offset:7296
	ds_read_b32 v180, v190 offset:7424
	ds_read_b32 v181, v190 offset:7552
	s_add_i32 s28, s40, 0
	s_mov_b32 s42, 0x60000
	s_mov_b32 m0, s28
	v_lshl_add_u64 v[186:187], v[188:189], 0, s[42:43]
	global_load_lds_dwordx4 v[186:187], off
	s_add_i32 s28, s40, 1024
	s_mov_b32 s42, 0x64000
	s_mov_b32 m0, s28
	v_lshl_add_u64 v[186:187], v[188:189], 0, s[42:43]
	global_load_lds_dwordx4 v[186:187], off
	s_add_i32 s28, s40, 2048
	s_mov_b32 s42, 0x68000
	s_mov_b32 m0, s28
	v_lshl_add_u64 v[186:187], v[188:189], 0, s[42:43]
	global_load_lds_dwordx4 v[186:187], off
	s_add_i32 s28, s40, 3072
	s_mov_b32 s42, 0x6c000
	s_mov_b32 m0, s28
	v_lshl_add_u64 v[186:187], v[188:189], 0, s[42:43]
	global_load_lds_dwordx4 v[186:187], off
	global_load_dwordx4 v[134:137], v[182:183], off offset:896
	global_load_dwordx4 v[150:153], v[184:185], off offset:896
	global_load_dwordx4 v[138:141], v[182:183], off offset:928
	global_load_dwordx4 v[154:157], v[184:185], off offset:928
	global_load_dwordx4 v[142:145], v[182:183], off offset:960
	global_load_dwordx4 v[158:161], v[184:185], off offset:960
	global_load_dwordx4 v[146:149], v[182:183], off offset:992
	global_load_dwordx4 v[162:165], v[184:185], off offset:992
	v_add_f32_e32 v38, v38, v54
	v_mul_f32_e32 v38, 0.5, v38
	v_add_f32_e32 v39, v39, v55
	v_mul_f32_e32 v39, 0.5, v39
	v_add_f32_e32 v40, v40, v56
	v_mul_f32_e32 v40, 0.5, v40
	s_waitcnt lgkmcnt(15)
	v_mfma_f32_32x32x2_f32 a[0:15], v38, v166, a[0:15]
	v_add_f32_e32 v41, v41, v57
	v_mul_f32_e32 v41, 0.5, v41
	s_waitcnt lgkmcnt(14)
	v_mfma_f32_32x32x2_f32 a[0:15], v39, v167, a[0:15]
	v_add_f32_e32 v42, v42, v58
	v_mul_f32_e32 v42, 0.5, v42
	s_waitcnt lgkmcnt(13)
	v_mfma_f32_32x32x2_f32 a[0:15], v40, v168, a[0:15]
	v_add_f32_e32 v43, v43, v59
	v_mul_f32_e32 v43, 0.5, v43
	s_waitcnt lgkmcnt(12)
	v_mfma_f32_32x32x2_f32 a[0:15], v41, v169, a[0:15]
	v_add_f32_e32 v44, v44, v60
	v_mul_f32_e32 v44, 0.5, v44
	s_waitcnt lgkmcnt(11)
	v_mfma_f32_32x32x2_f32 a[0:15], v42, v170, a[0:15]
	v_add_f32_e32 v45, v45, v61
	v_mul_f32_e32 v45, 0.5, v45
	s_waitcnt lgkmcnt(10)
	v_mfma_f32_32x32x2_f32 a[0:15], v43, v171, a[0:15]
	v_add_f32_e32 v46, v46, v62
	v_mul_f32_e32 v46, 0.5, v46
	s_waitcnt lgkmcnt(9)
	v_mfma_f32_32x32x2_f32 a[0:15], v44, v172, a[0:15]
	v_add_f32_e32 v47, v47, v63
	v_mul_f32_e32 v47, 0.5, v47
	s_waitcnt lgkmcnt(8)
	v_mfma_f32_32x32x2_f32 a[0:15], v45, v173, a[0:15]
	v_add_f32_e32 v48, v48, v64
	v_mul_f32_e32 v48, 0.5, v48
	s_waitcnt lgkmcnt(7)
	v_mfma_f32_32x32x2_f32 a[0:15], v46, v174, a[0:15]
	v_add_f32_e32 v49, v49, v65
	v_mul_f32_e32 v49, 0.5, v49
	s_waitcnt lgkmcnt(6)
	v_mfma_f32_32x32x2_f32 a[0:15], v47, v175, a[0:15]
	v_add_f32_e32 v50, v50, v66
	v_mul_f32_e32 v50, 0.5, v50
	s_waitcnt lgkmcnt(5)
	v_mfma_f32_32x32x2_f32 a[0:15], v48, v176, a[0:15]
	v_add_f32_e32 v51, v51, v67
	v_mul_f32_e32 v51, 0.5, v51
	s_waitcnt lgkmcnt(4)
	v_mfma_f32_32x32x2_f32 a[0:15], v49, v177, a[0:15]
	v_add_f32_e32 v52, v52, v68
	v_mul_f32_e32 v52, 0.5, v52
	s_waitcnt lgkmcnt(3)
	v_mfma_f32_32x32x2_f32 a[0:15], v50, v178, a[0:15]
	v_add_f32_e32 v53, v53, v69
	v_mul_f32_e32 v53, 0.5, v53
	s_waitcnt lgkmcnt(2)
	v_mfma_f32_32x32x2_f32 a[0:15], v51, v179, a[0:15]
	s_waitcnt lgkmcnt(1)
	v_mfma_f32_32x32x2_f32 a[0:15], v52, v180, a[0:15]
	s_waitcnt lgkmcnt(0)
	v_mfma_f32_32x32x2_f32 a[0:15], v53, v181, a[0:15]
	s_waitcnt vmcnt(20)
	ds_read_b32 v166, v190 offset:8192
	ds_read_b32 v167, v190 offset:8320
	ds_read_b32 v168, v190 offset:8448
	ds_read_b32 v169, v190 offset:8576
	ds_read_b32 v170, v190 offset:9216
	ds_read_b32 v171, v190 offset:9344
	ds_read_b32 v172, v190 offset:9472
	ds_read_b32 v173, v190 offset:9600
	ds_read_b32 v174, v190 offset:10240
	ds_read_b32 v175, v190 offset:10368
	ds_read_b32 v176, v190 offset:10496
	ds_read_b32 v177, v190 offset:10624
	ds_read_b32 v178, v190 offset:11264
	ds_read_b32 v179, v190 offset:11392
	ds_read_b32 v180, v190 offset:11520
	ds_read_b32 v181, v190 offset:11648
	s_add_i32 s28, s40, 4096
	s_mov_b32 s42, 0x70000
	s_mov_b32 m0, s28
	v_lshl_add_u64 v[186:187], v[188:189], 0, s[42:43]
	global_load_lds_dwordx4 v[186:187], off
	s_add_i32 s28, s40, 5120
	s_mov_b32 s42, 0x74000
	s_mov_b32 m0, s28
	v_lshl_add_u64 v[186:187], v[188:189], 0, s[42:43]
	global_load_lds_dwordx4 v[186:187], off
	s_add_i32 s28, s40, 6144
	s_mov_b32 s42, 0x78000
	s_mov_b32 m0, s28
	v_lshl_add_u64 v[186:187], v[188:189], 0, s[42:43]
	global_load_lds_dwordx4 v[186:187], off
	s_add_i32 s28, s40, 7168
	s_mov_b32 s42, 0x7c000
	s_mov_b32 m0, s28
	v_lshl_add_u64 v[186:187], v[188:189], 0, s[42:43]
	global_load_lds_dwordx4 v[186:187], off
	v_add_f32_e32 v70, v70, v86
	v_mul_f32_e32 v70, 0.5, v70
	v_add_f32_e32 v71, v71, v87
	v_mul_f32_e32 v71, 0.5, v71
	v_add_f32_e32 v72, v72, v88
	v_mul_f32_e32 v72, 0.5, v72
	s_waitcnt lgkmcnt(15)
	v_mfma_f32_32x32x2_f32 a[0:15], v70, v166, a[0:15]
	v_add_f32_e32 v73, v73, v89
	v_mul_f32_e32 v73, 0.5, v73
	s_waitcnt lgkmcnt(14)
	v_mfma_f32_32x32x2_f32 a[0:15], v71, v167, a[0:15]
	v_add_f32_e32 v74, v74, v90
	v_mul_f32_e32 v74, 0.5, v74
	s_waitcnt lgkmcnt(13)
	v_mfma_f32_32x32x2_f32 a[0:15], v72, v168, a[0:15]
	v_add_f32_e32 v75, v75, v91
	v_mul_f32_e32 v75, 0.5, v75
	s_waitcnt lgkmcnt(12)
	v_mfma_f32_32x32x2_f32 a[0:15], v73, v169, a[0:15]
	v_add_f32_e32 v76, v76, v92
	v_mul_f32_e32 v76, 0.5, v76
	s_waitcnt lgkmcnt(11)
	v_mfma_f32_32x32x2_f32 a[0:15], v74, v170, a[0:15]
	v_add_f32_e32 v77, v77, v93
	v_mul_f32_e32 v77, 0.5, v77
	s_waitcnt lgkmcnt(10)
	v_mfma_f32_32x32x2_f32 a[0:15], v75, v171, a[0:15]
	v_add_f32_e32 v78, v78, v94
	v_mul_f32_e32 v78, 0.5, v78
	s_waitcnt lgkmcnt(9)
	v_mfma_f32_32x32x2_f32 a[0:15], v76, v172, a[0:15]
	v_add_f32_e32 v79, v79, v95
	v_mul_f32_e32 v79, 0.5, v79
	s_waitcnt lgkmcnt(8)
	v_mfma_f32_32x32x2_f32 a[0:15], v77, v173, a[0:15]
	v_add_f32_e32 v80, v80, v96
	v_mul_f32_e32 v80, 0.5, v80
	s_waitcnt lgkmcnt(7)
	v_mfma_f32_32x32x2_f32 a[0:15], v78, v174, a[0:15]
	v_add_f32_e32 v81, v81, v97
	v_mul_f32_e32 v81, 0.5, v81
	s_waitcnt lgkmcnt(6)
	v_mfma_f32_32x32x2_f32 a[0:15], v79, v175, a[0:15]
	v_add_f32_e32 v82, v82, v98
	v_mul_f32_e32 v82, 0.5, v82
	s_waitcnt lgkmcnt(5)
	v_mfma_f32_32x32x2_f32 a[0:15], v80, v176, a[0:15]
	v_add_f32_e32 v83, v83, v99
	v_mul_f32_e32 v83, 0.5, v83
	s_waitcnt lgkmcnt(4)
	v_mfma_f32_32x32x2_f32 a[0:15], v81, v177, a[0:15]
	v_add_f32_e32 v84, v84, v100
	v_mul_f32_e32 v84, 0.5, v84
	s_waitcnt lgkmcnt(3)
	v_mfma_f32_32x32x2_f32 a[0:15], v82, v178, a[0:15]
	v_add_f32_e32 v85, v85, v101
	v_mul_f32_e32 v85, 0.5, v85
	s_waitcnt lgkmcnt(2)
	v_mfma_f32_32x32x2_f32 a[0:15], v83, v179, a[0:15]
	s_waitcnt lgkmcnt(1)
	v_mfma_f32_32x32x2_f32 a[0:15], v84, v180, a[0:15]
	s_waitcnt lgkmcnt(0)
	v_mfma_f32_32x32x2_f32 a[0:15], v85, v181, a[0:15]
	s_waitcnt vmcnt(12)
	ds_read_b32 v166, v190 offset:0
	ds_read_b32 v167, v190 offset:128
	ds_read_b32 v168, v190 offset:256
	ds_read_b32 v169, v190 offset:384
	ds_read_b32 v170, v190 offset:1024
	ds_read_b32 v171, v190 offset:1152
	ds_read_b32 v172, v190 offset:1280
	ds_read_b32 v173, v190 offset:1408
	ds_read_b32 v174, v190 offset:2048
	ds_read_b32 v175, v190 offset:2176
	ds_read_b32 v176, v190 offset:2304
	ds_read_b32 v177, v190 offset:2432
	ds_read_b32 v178, v190 offset:3072
	ds_read_b32 v179, v190 offset:3200
	ds_read_b32 v180, v190 offset:3328
	ds_read_b32 v181, v190 offset:3456
	v_add_f32_e32 v102, v102, v118
	v_mul_f32_e32 v102, 0.5, v102
	v_add_f32_e32 v103, v103, v119
	v_mul_f32_e32 v103, 0.5, v103
	v_add_f32_e32 v104, v104, v120
	v_mul_f32_e32 v104, 0.5, v104
	s_waitcnt lgkmcnt(15)
	v_mfma_f32_32x32x2_f32 a[0:15], v102, v166, a[0:15]
	v_add_f32_e32 v105, v105, v121
	v_mul_f32_e32 v105, 0.5, v105
	s_waitcnt lgkmcnt(14)
	v_mfma_f32_32x32x2_f32 a[0:15], v103, v167, a[0:15]
	v_add_f32_e32 v106, v106, v122
	v_mul_f32_e32 v106, 0.5, v106
	s_waitcnt lgkmcnt(13)
	v_mfma_f32_32x32x2_f32 a[0:15], v104, v168, a[0:15]
	v_add_f32_e32 v107, v107, v123
	v_mul_f32_e32 v107, 0.5, v107
	s_waitcnt lgkmcnt(12)
	v_mfma_f32_32x32x2_f32 a[0:15], v105, v169, a[0:15]
	v_add_f32_e32 v108, v108, v124
	v_mul_f32_e32 v108, 0.5, v108
	s_waitcnt lgkmcnt(11)
	v_mfma_f32_32x32x2_f32 a[0:15], v106, v170, a[0:15]
	v_add_f32_e32 v109, v109, v125
	v_mul_f32_e32 v109, 0.5, v109
	s_waitcnt lgkmcnt(10)
	v_mfma_f32_32x32x2_f32 a[0:15], v107, v171, a[0:15]
	v_add_f32_e32 v110, v110, v126
	v_mul_f32_e32 v110, 0.5, v110
	s_waitcnt lgkmcnt(9)
	v_mfma_f32_32x32x2_f32 a[0:15], v108, v172, a[0:15]
	v_add_f32_e32 v111, v111, v127
	v_mul_f32_e32 v111, 0.5, v111
	s_waitcnt lgkmcnt(8)
	v_mfma_f32_32x32x2_f32 a[0:15], v109, v173, a[0:15]
	v_add_f32_e32 v112, v112, v128
	v_mul_f32_e32 v112, 0.5, v112
	s_waitcnt lgkmcnt(7)
	v_mfma_f32_32x32x2_f32 a[0:15], v110, v174, a[0:15]
	v_add_f32_e32 v113, v113, v129
	v_mul_f32_e32 v113, 0.5, v113
	s_waitcnt lgkmcnt(6)
	v_mfma_f32_32x32x2_f32 a[0:15], v111, v175, a[0:15]
	v_add_f32_e32 v114, v114, v130
	v_mul_f32_e32 v114, 0.5, v114
	s_waitcnt lgkmcnt(5)
	v_mfma_f32_32x32x2_f32 a[0:15], v112, v176, a[0:15]
	v_add_f32_e32 v115, v115, v131
	v_mul_f32_e32 v115, 0.5, v115
	s_waitcnt lgkmcnt(4)
	v_mfma_f32_32x32x2_f32 a[0:15], v113, v177, a[0:15]
	v_add_f32_e32 v116, v116, v132
	v_mul_f32_e32 v116, 0.5, v116
	s_waitcnt lgkmcnt(3)
	v_mfma_f32_32x32x2_f32 a[0:15], v114, v178, a[0:15]
	v_add_f32_e32 v117, v117, v133
	v_mul_f32_e32 v117, 0.5, v117
	s_waitcnt lgkmcnt(2)
	v_mfma_f32_32x32x2_f32 a[0:15], v115, v179, a[0:15]
	s_waitcnt lgkmcnt(1)
	v_mfma_f32_32x32x2_f32 a[0:15], v116, v180, a[0:15]
	s_waitcnt lgkmcnt(0)
	v_mfma_f32_32x32x2_f32 a[0:15], v117, v181, a[0:15]
	s_waitcnt vmcnt(0)
	ds_read_b32 v166, v190 offset:4096
	ds_read_b32 v167, v190 offset:4224
	ds_read_b32 v168, v190 offset:4352
	ds_read_b32 v169, v190 offset:4480
	ds_read_b32 v170, v190 offset:5120
	ds_read_b32 v171, v190 offset:5248
	ds_read_b32 v172, v190 offset:5376
	ds_read_b32 v173, v190 offset:5504
	ds_read_b32 v174, v190 offset:6144
	ds_read_b32 v175, v190 offset:6272
	ds_read_b32 v176, v190 offset:6400
	ds_read_b32 v177, v190 offset:6528
	ds_read_b32 v178, v190 offset:7168
	ds_read_b32 v179, v190 offset:7296
	ds_read_b32 v180, v190 offset:7424
	ds_read_b32 v181, v190 offset:7552
	v_add_f32_e32 v134, v134, v150
	v_mul_f32_e32 v134, 0.5, v134
	v_add_f32_e32 v135, v135, v151
	v_mul_f32_e32 v135, 0.5, v135
	v_add_f32_e32 v136, v136, v152
	v_mul_f32_e32 v136, 0.5, v136
	s_waitcnt lgkmcnt(15)
	v_mfma_f32_32x32x2_f32 a[0:15], v134, v166, a[0:15]
	v_add_f32_e32 v137, v137, v153
	v_mul_f32_e32 v137, 0.5, v137
	s_waitcnt lgkmcnt(14)
	v_mfma_f32_32x32x2_f32 a[0:15], v135, v167, a[0:15]
	v_add_f32_e32 v138, v138, v154
	v_mul_f32_e32 v138, 0.5, v138
	s_waitcnt lgkmcnt(13)
	v_mfma_f32_32x32x2_f32 a[0:15], v136, v168, a[0:15]
	v_add_f32_e32 v139, v139, v155
	v_mul_f32_e32 v139, 0.5, v139
	s_waitcnt lgkmcnt(12)
	v_mfma_f32_32x32x2_f32 a[0:15], v137, v169, a[0:15]
	v_add_f32_e32 v140, v140, v156
	v_mul_f32_e32 v140, 0.5, v140
	s_waitcnt lgkmcnt(11)
	v_mfma_f32_32x32x2_f32 a[0:15], v138, v170, a[0:15]
	v_add_f32_e32 v141, v141, v157
	v_mul_f32_e32 v141, 0.5, v141
	s_waitcnt lgkmcnt(10)
	v_mfma_f32_32x32x2_f32 a[0:15], v139, v171, a[0:15]
	v_add_f32_e32 v142, v142, v158
	v_mul_f32_e32 v142, 0.5, v142
	s_waitcnt lgkmcnt(9)
	v_mfma_f32_32x32x2_f32 a[0:15], v140, v172, a[0:15]
	v_add_f32_e32 v143, v143, v159
	v_mul_f32_e32 v143, 0.5, v143
	s_waitcnt lgkmcnt(8)
	v_mfma_f32_32x32x2_f32 a[0:15], v141, v173, a[0:15]
	v_add_f32_e32 v144, v144, v160
	v_mul_f32_e32 v144, 0.5, v144
	s_waitcnt lgkmcnt(7)
	v_mfma_f32_32x32x2_f32 a[0:15], v142, v174, a[0:15]
	v_add_f32_e32 v145, v145, v161
	v_mul_f32_e32 v145, 0.5, v145
	s_waitcnt lgkmcnt(6)
	v_mfma_f32_32x32x2_f32 a[0:15], v143, v175, a[0:15]
	v_add_f32_e32 v146, v146, v162
	v_mul_f32_e32 v146, 0.5, v146
	s_waitcnt lgkmcnt(5)
	v_mfma_f32_32x32x2_f32 a[0:15], v144, v176, a[0:15]
	v_add_f32_e32 v147, v147, v163
	v_mul_f32_e32 v147, 0.5, v147
	s_waitcnt lgkmcnt(4)
	v_mfma_f32_32x32x2_f32 a[0:15], v145, v177, a[0:15]
	v_add_f32_e32 v148, v148, v164
	v_mul_f32_e32 v148, 0.5, v148
	s_waitcnt lgkmcnt(3)
	v_mfma_f32_32x32x2_f32 a[0:15], v146, v178, a[0:15]
	v_add_f32_e32 v149, v149, v165
	v_mul_f32_e32 v149, 0.5, v149
	s_waitcnt lgkmcnt(2)
	v_mfma_f32_32x32x2_f32 a[0:15], v147, v179, a[0:15]
	s_waitcnt lgkmcnt(1)
	v_mfma_f32_32x32x2_f32 a[0:15], v148, v180, a[0:15]
	s_waitcnt lgkmcnt(0)
	v_mfma_f32_32x32x2_f32 a[0:15], v149, v181, a[0:15]
	s_mov_b32 s30, 0x80000
	s_mov_b32 s31, 0
	s_nop 1
	s_lshl_b32 s28, s34, 5
	s_and_b32 s28, s28, 0x1e0
	v_or_b32_e32 v14, s28, v2
	v_lshlrev_b32_e32 v14, 2, v14
	s_nop 12
	ds_write_b32 v3, a0
	ds_write_b32 v3, a1 offset:256
	ds_write_b32 v3, a2 offset:512
	ds_write_b32 v3, a3 offset:768
	ds_write_b32 v3, a4 offset:1024
	ds_write_b32 v3, a5 offset:1280
	ds_write_b32 v3, a6 offset:1536
	ds_write_b32 v3, a7 offset:1792
	ds_write_b32 v3, a8 offset:2048
	ds_write_b32 v3, a9 offset:2304
	ds_write_b32 v3, a10 offset:2560
	ds_write_b32 v3, a11 offset:2816
	ds_write_b32 v3, a12 offset:3072
	ds_write_b32 v3, a13 offset:3328
	ds_write_b32 v3, a14 offset:3584
	ds_write_b32 v3, a15 offset:3840
	s_waitcnt lgkmcnt(0)
	s_barrier
	global_load_dword v37, v14, s[22:23]
	global_load_dword v42, v14, s[26:27]
	ds_read2st64_b32 v[14:15], v28 offset1:4
	ds_read2st64_b32 v[16:17], v28 offset0:16 offset1:20
	ds_read2st64_b32 v[18:19], v28 offset0:32 offset1:36
	ds_read2st64_b32 v[20:21], v28 offset0:48 offset1:52
	ds_read2st64_b32 v[22:23], v28 offset0:8 offset1:12
	ds_read2st64_b32 v[24:25], v28 offset0:24 offset1:28
	ds_read2st64_b32 v[38:39], v28 offset0:40 offset1:44
	ds_read2st64_b32 v[40:41], v28 offset0:56 offset1:60
	s_waitcnt lgkmcnt(6)
	v_add_f32_e32 v14, v14, v16
	v_add_f32_e32 v15, v15, v17
	s_waitcnt lgkmcnt(5)
	v_add_f32_e32 v14, v14, v18
	s_waitcnt lgkmcnt(2)
	v_add_f32_e32 v16, v22, v24
	v_add_f32_e32 v15, v15, v19
	v_add_f32_e32 v14, v14, v20
	v_add_f32_e32 v17, v23, v25
	s_waitcnt lgkmcnt(1)
	v_add_f32_e32 v16, v16, v38
	v_add_f32_e32 v15, v15, v21
	v_add_f32_e32 v17, v17, v39
	s_waitcnt lgkmcnt(0)
	v_add_f32_e32 v16, v16, v40
	v_add_f32_e32 v17, v17, v41
	v_cmp_lt_i32_e32 vcc, v31, v30
	s_waitcnt vmcnt(1)
	v_add_f32_e32 v14, v14, v37
	v_add_f32_e32 v15, v15, v37
	v_max_f32_e32 v14, 0, v14
	v_add_f32_e32 v16, v16, v37
	v_max_f32_e32 v15, 0, v15
	s_waitcnt vmcnt(0)
	v_fma_f32 v14, v42, v14, 0
	v_add_f32_e32 v17, v17, v37
	v_max_f32_e32 v16, 0, v16
	v_fmac_f32_e32 v14, v42, v15
	v_cndmask_b32_e32 v43, v29, v31, vcc
	v_max_f32_e32 v17, 0, v17
	v_fmac_f32_e32 v14, v42, v16
	v_lshlrev_b32_e32 v43, 2, v43
	v_fmac_f32_e32 v14, v42, v17
	ds_bpermute_b32 v15, v43, v14
	v_cmp_lt_i32_e32 vcc, v32, v30
	s_waitcnt lgkmcnt(0)
	v_add_f32_e32 v14, v14, v15
	v_cndmask_b32_e32 v16, v29, v32, vcc
	v_lshlrev_b32_e32 v16, 2, v16
	ds_bpermute_b32 v15, v16, v14
	v_cmp_lt_i32_e32 vcc, v33, v30
	s_waitcnt lgkmcnt(0)
	v_add_f32_e32 v14, v14, v15
	v_cndmask_b32_e32 v16, v29, v33, vcc
	v_lshlrev_b32_e32 v16, 2, v16
	ds_bpermute_b32 v15, v16, v14
	v_cmp_lt_i32_e32 vcc, v34, v30
	s_waitcnt lgkmcnt(0)
	v_add_f32_e32 v14, v14, v15
	v_cndmask_b32_e32 v16, v29, v34, vcc
	v_lshlrev_b32_e32 v16, 2, v16
	ds_bpermute_b32 v15, v16, v14
	v_cmp_lt_i32_e32 vcc, v35, v30
	s_waitcnt lgkmcnt(0)
	v_add_f32_e32 v14, v14, v15
	v_cndmask_b32_e32 v16, v29, v35, vcc
	v_lshlrev_b32_e32 v16, 2, v16
	ds_bpermute_b32 v15, v16, v14
	v_cmp_lt_i32_e32 vcc, v36, v30
	s_waitcnt lgkmcnt(0)
	v_add_f32_e32 v14, v14, v15
	v_cndmask_b32_e32 v16, v29, v36, vcc
	v_lshlrev_b32_e32 v15, 2, v16
	ds_bpermute_b32 v15, v15, v14
	s_and_saveexec_b64 s[30:31], s[8:9]
	s_cbranch_execz .LBB2_18
	s_waitcnt lgkmcnt(0)
	v_add_f32_e32 v14, v14, v15
	ds_write_b32 v27, v14

	.amdhsa_kernel _Z20refine_gather_kernelPKfS0_S0_S0_S0_S0_S0_PfPiS1_
		.amdhsa_group_segment_fixed_size 65600
		.amdhsa_private_segment_fixed_size 0
		.amdhsa_kernarg_size 80
		.amdhsa_user_sgpr_count 2
		.amdhsa_user_sgpr_dispatch_ptr 0
		.amdhsa_user_sgpr_queue_ptr 0
		.amdhsa_user_sgpr_kernarg_segment_ptr 1
		.amdhsa_user_sgpr_dispatch_id 0
		.amdhsa_user_sgpr_kernarg_preload_length 0
		.amdhsa_user_sgpr_kernarg_preload_offset 0
		.amdhsa_user_sgpr_private_segment_size 0
		.amdhsa_uses_dynamic_stack 0
		.amdhsa_enable_private_segment 0
		.amdhsa_system_sgpr_workgroup_id_x 1
		.amdhsa_system_sgpr_workgroup_id_y 0
		.amdhsa_system_sgpr_workgroup_id_z 0
		.amdhsa_system_sgpr_workgroup_info 0
		.amdhsa_system_vgpr_workitem_id 0
		.amdhsa_next_free_vgpr 208
		.amdhsa_next_free_sgpr 100
		.amdhsa_accum_offset 192
		.amdhsa_reserve_vcc 1
		.amdhsa_float_round_mode_32 0
		.amdhsa_float_round_mode_16_64 0
		.amdhsa_float_denorm_mode_32 3
		.amdhsa_float_denorm_mode_16_64 3
		.amdhsa_dx10_clamp 1
		.amdhsa_ieee_mode 1
		.amdhsa_fp16_overflow 0
		.amdhsa_tg_split 0
		.amdhsa_exception_fp_ieee_invalid_op 0
		.amdhsa_exception_fp_denorm_src 0
		.amdhsa_exception_fp_ieee_div_zero 0
		.amdhsa_exception_fp_ieee_overflow 0
		.amdhsa_exception_fp_ieee_underflow 0
		.amdhsa_exception_fp_ieee_inexact 0
		.amdhsa_exception_int_div_zero 0
	.end_amdhsa_kernel

amdhsa.kernels:
  - .agpr_count:     0
    .args:
      - .actual_access:  read_only
        .address_space:  global
        .offset:         0
        .size:           8
        .value_kind:     global_buffer
      - .actual_access:  write_only
        .address_space:  global
        .offset:         8
        .size:           8
        .value_kind:     global_buffer
    .group_segment_fixed_size: 0
    .kernarg_segment_align: 8
    .kernarg_segment_size: 16
    .language:       OpenCL C
    .language_version:
      - 2
      - 0
    .max_flat_workgroup_size: 256
    .name:           _Z7prep_w1PKfPDv8_DF16_
    .private_segment_fixed_size: 0
    .sgpr_count:     14
    .sgpr_spill_count: 0
    .symbol:         _Z7prep_w1PKfPDv8_DF16_.kd
    .uniform_work_group_size: 1
    .uses_dynamic_stack: false
    .vgpr_count:     26
    .vgpr_spill_count: 0
    .wavefront_size: 64
  - .agpr_count:     0
    .args:
      - .address_space:  global
        .offset:         0
        .size:           8
        .value_kind:     global_buffer
      - .address_space:  global
        .offset:         8
        .size:           8
        .value_kind:     global_buffer
      - .address_space:  global
        .offset:         16
        .size:           8
        .value_kind:     global_buffer
      - .actual_access:  read_only
        .address_space:  global
        .offset:         24
        .size:           8
        .value_kind:     global_buffer
      - .actual_access:  read_only
        .address_space:  global
        .offset:         32
        .size:           8
        .value_kind:     global_buffer
      - .actual_access:  write_only
        .address_space:  global
        .offset:         40
        .size:           8
        .value_kind:     global_buffer
      - .actual_access:  write_only
        .address_space:  global
        .offset:         48
        .size:           8
        .value_kind:     global_buffer
    .group_segment_fixed_size: 163840
    .kernarg_segment_align: 8
    .kernarg_segment_size: 56
    .language:       OpenCL C
    .language_version:
      - 2
      - 0
    .max_flat_workgroup_size: 768
    .name:           _Z12score_kernelPKfS0_PKcS0_S0_PfPi
    .private_segment_fixed_size: 0
    .sgpr_count:     34
    .sgpr_spill_count: 0
    .symbol:         _Z12score_kernelPKfS0_PKcS0_S0_PfPi.kd
    .uniform_work_group_size: 1
    .uses_dynamic_stack: false
    .vgpr_count:     164
    .vgpr_spill_count: 0
    .wavefront_size: 64
  - .agpr_count:     16
    .args:
      - .actual_access:  read_only
        .address_space:  global
        .offset:         0
        .size:           8
        .value_kind:     global_buffer
      - .actual_access:  read_only
        .address_space:  global
        .offset:         8
        .size:           8
        .value_kind:     global_buffer
      - .actual_access:  read_only
        .address_space:  global
        .offset:         16
        .size:           8
        .value_kind:     global_buffer
      - .actual_access:  read_only
        .address_space:  global
        .offset:         24
        .size:           8
        .value_kind:     global_buffer
      - .actual_access:  read_only
        .address_space:  global
        .offset:         32
        .size:           8
        .value_kind:     global_buffer
      - .actual_access:  read_only
        .address_space:  global
        .offset:         40
        .size:           8
        .value_kind:     global_buffer
      - .actual_access:  read_only
        .address_space:  global
        .offset:         48
        .size:           8
        .value_kind:     global_buffer
      - .address_space:  global
        .offset:         56
        .size:           8
        .value_kind:     global_buffer
      - .address_space:  global
        .offset:         64
        .size:           8
        .value_kind:     global_buffer
      - .actual_access:  write_only
        .address_space:  global
        .offset:         72
        .size:           8
        .value_kind:     global_buffer
    .group_segment_fixed_size: 65600
    .kernarg_segment_align: 8
    .kernarg_segment_size: 80
    .language:       OpenCL C
    .language_version:
      - 2
      - 0
    .max_flat_workgroup_size: 256
    .name:           _Z20refine_gather_kernelPKfS0_S0_S0_S0_S0_S0_PfPiS1_
    .private_segment_fixed_size: 0
    .sgpr_count:     106
    .sgpr_spill_count: 94
    .symbol:         _Z20refine_gather_kernelPKfS0_S0_S0_S0_S0_S0_PfPiS1_.kd
    .uniform_work_group_size: 1
    .uses_dynamic_stack: false
    .vgpr_count:     208
    .vgpr_spill_count: 0
    .wavefront_size: 64
